# baseline (speedup 1.0000x reference)
.LBB8_2:
	s_or_b64 exec, exec, s[10:11]
	s_barrier
	s_load_dword s10, s[0:1], 0x4
	s_waitcnt lgkmcnt(0)
	s_add_i32 s3, s10, s3
	s_lshl_b32 s16, s3, 4
	s_cmp_ge_i32 s16, s2
	s_cbranch_scc1 .LBB8_11
	s_cmpk_gt_i32 s3, 0xff
	s_cselect_b64 s[10:11], -1, 0

.LBB8_4:
	s_lshl_b32 s16, s3, 4
	s_waitcnt vmcnt(0)
	v_or_b32_e32 v0, s16, v28
	v_ashrrev_i32_e32 v1, 31, v0
	v_lshl_add_u64 v[0:1], v[0:1], 2, s[24:25]
	global_load_dword v0, v[0:1], off
	s_waitcnt lgkmcnt(0)
	s_cmp_ge_i32 s16, s2
	s_cbranch_scc1 .LBB8_11
	v_or_b32_e32 v22, s16, v29
	v_mov_b32_e32 v23, v21
	s_and_saveexec_b64 s[10:11], s[4:5]
	s_cbranch_execnz .LBB8_6
	s_or_b64 exec, exec, s[10:11]
	s_waitcnt lgkmcnt(0)
	s_cmp_ge_i32 s16, s2
	s_mov_b64 s[10:11], -1
	s_cbranch_scc1 .LBB8_3
	s_branch .LBB8_7

.LBB9_2:
	s_or_b64 exec, exec, s[18:19]
	s_barrier
	s_load_dword s18, s[0:1], 0x4
	s_waitcnt lgkmcnt(0)
	s_add_i32 s3, s18, s3
	s_lshl_b32 s23, s3, 4
	s_cmp_ge_i32 s23, s2
	s_cbranch_scc1 .LBB9_9
	s_cmpk_gt_i32 s3, 0xff
	s_cselect_b64 s[18:19], -1, 0

.LBB9_6:
	s_or_b64 exec, exec, s[18:19]
	s_lshl_b32 s23, s3, 4
	v_or_b32_e32 v49, s23, v44
	v_mad_i64_i32 v[50:51], s[18:19], v49, s22, 0
	v_lshl_add_u64 v[58:59], v[50:51], 2, s[20:21]
	v_lshl_add_u64 v[60:61], v[4:5], 2, v[58:59]
	v_lshl_add_u64 v[62:63], v[14:15], 2, v[58:59]
	global_load_dwordx4 v[50:53], v[60:61], off
	global_load_dwordx4 v[54:57], v[62:63], off
	global_load_dword v66, v[6:7], off
	global_load_dword v70, v[8:9], off
	global_load_dword v71, v[10:11], off
	global_load_dword v72, v[12:13], off
	global_load_dword v73, v[16:17], off
	global_load_dword v74, v[18:19], off
	global_load_dword v75, v[20:21], off
	global_load_dword v76, v[22:23], off
	v_lshl_add_u64 v[60:61], v[24:25], 2, v[58:59]
	v_lshl_add_u64 v[62:63], v[34:35], 2, v[58:59]
	global_load_dwordx4 v[58:61], v[60:61], off
	s_nop 0
	global_load_dwordx4 v[62:65], v[62:63], off
	s_nop 0
	global_load_dword v77, v[26:27], off
	global_load_dword v78, v[28:29], off
	global_load_dword v79, v[30:31], off
	global_load_dword v80, v[32:33], off
	global_load_dword v81, v[36:37], off
	global_load_dword v82, v[38:39], off
	global_load_dword v83, v[40:41], off
	global_load_dword v84, v[42:43], off
	s_waitcnt lgkmcnt(0)
	s_cmp_ge_i32 s23, s2
	s_mov_b64 s[18:19], -1
	s_cbranch_scc1 .LBB9_3
	v_or_b32_e32 v49, s23, v45
	s_waitcnt vmcnt(19)
	v_cndmask_b32_e64 v50, 0, v50, s[6:7]
	s_waitcnt vmcnt(18)
	v_cndmask_b32_e64 v54, 0, v54, s[8:9]
	v_cmp_le_i32_e32 vcc, s2, v49
	s_or_b64 s[18:19], s[16:17], vcc
	s_nor_b64 s[24:25], s[18:19], s[14:15]
	s_waitcnt vmcnt(17)
	v_mfma_f32_16x16x4_f32 v[66:69], v50, v66, 0
	v_cndmask_b32_e64 v50, 0, v51, s[6:7]
	s_waitcnt vmcnt(16)
	s_nop 0
	v_mfma_f32_16x16x4_f32 v[66:69], v50, v70, v[66:69]
	v_cndmask_b32_e64 v50, 0, v52, s[6:7]
	s_waitcnt vmcnt(15)
	s_nop 0
	v_mfma_f32_16x16x4_f32 v[66:69], v50, v71, v[66:69]
	v_cndmask_b32_e64 v50, 0, v53, s[6:7]
	s_waitcnt vmcnt(14)
	s_nop 0
	v_mfma_f32_16x16x4_f32 v[50:53], v50, v72, v[66:69]
	s_waitcnt vmcnt(13)
	v_mfma_f32_16x16x4_f32 v[50:53], v54, v73, v[50:53]
	v_cndmask_b32_e64 v54, 0, v55, s[8:9]
	s_waitcnt vmcnt(12)
	s_nop 0
	v_mfma_f32_16x16x4_f32 v[50:53], v54, v74, v[50:53]
	v_cndmask_b32_e64 v54, 0, v56, s[8:9]
	s_waitcnt vmcnt(11)
	s_nop 0
	v_mfma_f32_16x16x4_f32 v[50:53], v54, v75, v[50:53]
	v_cndmask_b32_e64 v54, 0, v57, s[8:9]
	s_waitcnt vmcnt(10)
	s_nop 0
	v_mfma_f32_16x16x4_f32 v[50:53], v54, v76, v[50:53]
	s_waitcnt vmcnt(9)
	v_cndmask_b32_e64 v54, 0, v58, s[10:11]
	s_waitcnt vmcnt(7)
	s_nop 0
	v_mfma_f32_16x16x4_f32 v[50:53], v54, v77, v[50:53]
	v_cndmask_b32_e64 v54, 0, v59, s[10:11]
	s_waitcnt vmcnt(6)
	s_nop 0
	v_mfma_f32_16x16x4_f32 v[50:53], v54, v78, v[50:53]
	v_cndmask_b32_e64 v54, 0, v60, s[10:11]
	s_waitcnt vmcnt(5)
	s_nop 0
	v_mfma_f32_16x16x4_f32 v[50:53], v54, v79, v[50:53]
	v_cndmask_b32_e64 v54, 0, v61, s[10:11]
	s_waitcnt vmcnt(4)
	s_nop 0
	v_mfma_f32_16x16x4_f32 v[50:53], v54, v80, v[50:53]
	v_cndmask_b32_e64 v54, 0, v62, s[12:13]
	s_waitcnt vmcnt(3)
	s_nop 0
	v_mfma_f32_16x16x4_f32 v[50:53], v54, v81, v[50:53]
	v_cndmask_b32_e64 v54, 0, v63, s[12:13]
	s_waitcnt vmcnt(2)
	s_nop 0
	v_mfma_f32_16x16x4_f32 v[50:53], v54, v82, v[50:53]
	v_cndmask_b32_e64 v54, 0, v64, s[12:13]
	s_waitcnt vmcnt(1)
	s_nop 0
	v_mfma_f32_16x16x4_f32 v[50:53], v54, v83, v[50:53]
	v_cndmask_b32_e64 v54, 0, v65, s[12:13]
	s_waitcnt vmcnt(0)
	s_nop 0
	v_mfma_f32_16x16x4_f32 v[50:53], v54, v84, v[50:53]
	s_nop 9
	ds_write2st64_b32 v46, v50, v51 offset1:1
	ds_write2st64_b32 v46, v52, v53 offset0:2 offset1:3
	s_waitcnt lgkmcnt(0)
	s_barrier
	s_and_saveexec_b64 s[18:19], s[24:25]
	s_cbranch_execz .LBB9_2
	ds_read2st64_b32 v[50:51], v47 offset1:4
	ds_read2st64_b32 v[52:53], v47 offset0:8 offset1:12
	ds_read2st64_b32 v[54:55], v47 offset0:16 offset1:20
	ds_read2st64_b32 v[56:57], v47 offset0:24 offset1:28
	ds_read2st64_b32 v[58:59], v47 offset0:32 offset1:36
	s_waitcnt lgkmcnt(4)
	v_add_f32_e32 v50, 0, v50
	v_add_f32_e32 v50, v50, v51
	s_waitcnt lgkmcnt(3)
	v_add_f32_e32 v50, v50, v52
	v_add_f32_e32 v50, v50, v53
	s_waitcnt lgkmcnt(2)
	v_add_f32_e32 v50, v50, v54
	v_add_f32_e32 v50, v50, v55
	s_waitcnt lgkmcnt(1)
	v_add_f32_e32 v50, v50, v56
	v_add_f32_e32 v52, v50, v57
	ds_read2st64_b32 v[50:51], v47 offset0:40 offset1:44
	s_waitcnt lgkmcnt(1)
	v_add_f32_e32 v54, v52, v58
	ds_read2st64_b32 v[52:53], v47 offset0:48 offset1:52
	v_add_f32_e32 v56, v54, v59
	ds_read2st64_b32 v[54:55], v47 offset0:56 offset1:60
	s_waitcnt lgkmcnt(2)
	v_add_f32_e32 v50, v56, v50
	v_add_f32_e32 v50, v50, v51
	s_waitcnt lgkmcnt(1)
	v_add_f32_e32 v50, v50, v52
	v_add_f32_e32 v50, v50, v53
	s_waitcnt lgkmcnt(0)
	v_add_f32_e32 v50, v50, v54
	v_add_f32_e32 v50, v50, v55
	v_add_f32_e32 v48, v48, v50
	v_max_f32_e32 v50, 0, v48
	v_mad_i64_i32 v[48:49], s[24:25], v49, s28, 0
	v_lshl_add_u64 v[48:49], v[48:49], 2, v[0:1]
	global_store_dword v[48:49], v50, off
	s_branch .LBB9_2

.LBB10_2:
	s_or_b64 exec, exec, s[22:23]
	s_barrier
	s_load_dword s19, s[0:1], 0x4
	s_waitcnt lgkmcnt(0)
	s_add_i32 s3, s19, s3
	s_lshl_b32 s19, s3, 4
	s_cmp_ge_i32 s19, s2
	s_cbranch_scc1 .LBB10_12
	s_cmpk_gt_i32 s3, 0xff
	s_cselect_b64 s[22:23], -1, 0

.LBB10_4:
	s_lshl_b32 s19, s3, 4
	v_or_b32_e32 v46, s19, v49
	v_mov_b64_e32 v[44:45], 0
	s_waitcnt vmcnt(0)
	v_mov_b32_e32 v1, 0
	s_and_saveexec_b64 s[22:23], s[12:13]
	s_cbranch_execnz .LBB10_6
	s_or_b64 exec, exec, s[22:23]
	s_branch .LBB10_7

.LBB10_7:
	v_or_b32_e32 v47, s19, v48
	v_mad_i64_i32 v[54:55], s[22:23], v47, s18, 0
	v_lshl_add_u64 v[62:63], v[54:55], 2, s[16:17]
	v_lshl_add_u64 v[64:65], v[4:5], 2, v[62:63]
	v_lshl_add_u64 v[66:67], v[14:15], 2, v[62:63]
	v_lshl_add_u64 v[70:71], v[24:25], 2, v[62:63]
	global_load_dwordx4 v[54:57], v[64:65], off
	global_load_dwordx4 v[58:61], v[66:67], off
	global_load_dword v47, v[6:7], off
	global_load_dword v53, v[8:9], off
	global_load_dword v74, v[10:11], off
	global_load_dword v75, v[12:13], off
	global_load_dword v76, v[16:17], off
	global_load_dword v77, v[18:19], off
	global_load_dword v78, v[20:21], off
	global_load_dword v79, v[22:23], off
	v_lshl_add_u64 v[72:73], v[34:35], 2, v[62:63]
	global_load_dwordx4 v[62:65], v[70:71], off
	global_load_dwordx4 v[66:69], v[72:73], off
	global_load_dword v80, v[26:27], off
	global_load_dword v81, v[28:29], off
	global_load_dword v82, v[30:31], off
	global_load_dword v83, v[32:33], off
	global_load_dword v84, v[36:37], off
	global_load_dword v85, v[38:39], off
	global_load_dword v86, v[40:41], off
	global_load_dword v87, v[42:43], off
	s_waitcnt lgkmcnt(0)
	s_cmp_ge_i32 s19, s2
	s_mov_b64 s[22:23], -1
	s_cbranch_scc1 .LBB10_3
	s_waitcnt vmcnt(19)
	v_cndmask_b32_e64 v54, 0, v54, s[4:5]
	s_waitcnt vmcnt(17)
	s_nop 0
	v_mfma_f32_16x16x4_f32 v[70:73], v54, v47, 0
	v_cndmask_b32_e64 v47, 0, v55, s[4:5]
	s_waitcnt vmcnt(16)
	s_nop 0
	v_mfma_f32_16x16x4_f32 v[70:73], v47, v53, v[70:73]
	v_cndmask_b32_e64 v47, 0, v56, s[4:5]
	s_waitcnt vmcnt(15)
	s_nop 0
	v_mfma_f32_16x16x4_f32 v[70:73], v47, v74, v[70:73]
	v_cndmask_b32_e64 v47, 0, v57, s[4:5]
	s_waitcnt vmcnt(14)
	s_nop 0
	v_mfma_f32_16x16x4_f32 v[54:57], v47, v75, v[70:73]
	v_cndmask_b32_e64 v47, 0, v58, s[6:7]
	s_waitcnt vmcnt(13)
	s_nop 0
	v_mfma_f32_16x16x4_f32 v[54:57], v47, v76, v[54:57]
	v_cndmask_b32_e64 v47, 0, v59, s[6:7]
	s_waitcnt vmcnt(12)
	s_nop 0
	v_mfma_f32_16x16x4_f32 v[54:57], v47, v77, v[54:57]
	v_cndmask_b32_e64 v47, 0, v60, s[6:7]
	s_waitcnt vmcnt(11)
	s_nop 0
	v_mfma_f32_16x16x4_f32 v[54:57], v47, v78, v[54:57]
	v_cndmask_b32_e64 v47, 0, v61, s[6:7]
	s_waitcnt vmcnt(10)
	s_nop 0
	v_mfma_f32_16x16x4_f32 v[54:57], v47, v79, v[54:57]
	s_waitcnt vmcnt(9)
	v_cndmask_b32_e64 v47, 0, v62, s[8:9]
	s_waitcnt vmcnt(7)
	s_nop 0
	v_mfma_f32_16x16x4_f32 v[54:57], v47, v80, v[54:57]
	v_cndmask_b32_e64 v47, 0, v63, s[8:9]
	s_waitcnt vmcnt(6)
	s_nop 0
	v_mfma_f32_16x16x4_f32 v[54:57], v47, v81, v[54:57]
	v_cndmask_b32_e64 v47, 0, v64, s[8:9]
	s_waitcnt vmcnt(5)
	s_nop 0
	v_mfma_f32_16x16x4_f32 v[54:57], v47, v82, v[54:57]
	v_cndmask_b32_e64 v47, 0, v65, s[8:9]
	s_waitcnt vmcnt(4)
	s_nop 0
	v_mfma_f32_16x16x4_f32 v[54:57], v47, v83, v[54:57]
	v_cndmask_b32_e64 v47, 0, v66, s[10:11]
	s_waitcnt vmcnt(3)
	s_nop 0
	v_mfma_f32_16x16x4_f32 v[54:57], v47, v84, v[54:57]
	v_cndmask_b32_e64 v47, 0, v67, s[10:11]
	s_waitcnt vmcnt(2)
	s_nop 0
	v_mfma_f32_16x16x4_f32 v[54:57], v47, v85, v[54:57]
	v_cndmask_b32_e64 v47, 0, v68, s[10:11]
	s_waitcnt vmcnt(1)
	s_nop 0
	v_mfma_f32_16x16x4_f32 v[54:57], v47, v86, v[54:57]
	v_cndmask_b32_e64 v47, 0, v69, s[10:11]
	s_waitcnt vmcnt(0)
	s_nop 0
	v_mfma_f32_16x16x4_f32 v[54:57], v47, v87, v[54:57]
	s_nop 9
	ds_write2st64_b32 v50, v54, v55 offset1:1
	ds_write2st64_b32 v50, v56, v57 offset0:2 offset1:3
	s_waitcnt lgkmcnt(0)
	s_barrier
	s_and_saveexec_b64 s[22:23], s[12:13]
	s_cbranch_execz .LBB10_2
	v_cmp_gt_i32_e32 vcc, s2, v46
	s_and_b64 s[30:31], vcc, s[20:21]
	v_mov_b64_e32 v[46:47], 0
	s_and_saveexec_b64 s[26:27], s[30:31]
	s_cbranch_execz .LBB10_10
	ds_read2st64_b32 v[46:47], v51 offset1:4
	ds_read2st64_b32 v[54:55], v51 offset0:8 offset1:12
	ds_read2st64_b32 v[56:57], v51 offset0:16 offset1:20
	ds_read2st64_b32 v[58:59], v51 offset0:24 offset1:28
	s_waitcnt lgkmcnt(3)
	v_add_f32_e32 v46, 0, v46
	v_add_f32_e32 v46, v46, v47
	s_waitcnt lgkmcnt(2)
	v_add_f32_e32 v46, v46, v54
	v_add_f32_e32 v46, v46, v55
	s_waitcnt lgkmcnt(1)
	v_add_f32_e32 v46, v46, v56
	v_add_f32_e32 v46, v46, v57
	s_waitcnt lgkmcnt(0)
	v_add_f32_e32 v46, v46, v58
	v_add_f32_e32 v46, v46, v59
	v_add_f32_e32 v1, v1, v46
	v_not_b32_e32 v46, v1
	v_or_b32_e32 v47, 0x80000000, v1
	v_cmp_gt_i32_e32 vcc, 0, v1
	s_nop 1
	v_cndmask_b32_e32 v1, v47, v46, vcc
	v_mov_b64_e32 v[46:47], v[0:1]
